# stack: P1 + P14 K-loop LDS-DMA in SGPR-base form, P14 stage loads 4+4, P8 ladder pipelined + deferred stores, P7 gain hoist
# baseline (speedup 1.0000x reference)
.LBB0_216:
	v_add_u32_e32 v130, s88, v196
	v_add_u32_e32 v134, s89, v196
	ds_read_b128 v[158:161], v130
	ds_read_b128 v[150:153], v130 offset:1024
	ds_read_b128 v[154:157], v130 offset:2048
	ds_read_b128 v[146:149], v130 offset:3072
	ds_read_b128 v[142:145], v134
	ds_read_b128 v[130:133], v134 offset:1024
	ds_read_b128 v[138:141], v134 offset:2048
	ds_read_b128 v[134:137], v134 offset:3072
	s_add_u32 s25, s50, 0xfff80080
	s_addc_u32 s56, s51, -1
	s_and_b64 s[18:19], s[18:19], exec
	s_cselect_b32 s59, s31, s56
	s_cselect_b32 s58, s4, s25
	s_cselect_b32 s57, s5, s64
	s_cselect_b32 s56, s29, s92
	s_add_i32 m0, s39, 0xc000
	ds_read_b128 v[186:189], v198
	ds_read_b128 v[190:193], v198 offset:1024
	ds_read_b128 v[200:203], v198 offset:2048
	ds_read_b128 v[204:207], v198 offset:3072
	ds_read_b128 v[208:211], v198 offset:4096
	ds_read_b128 v[212:215], v198 offset:5120
	ds_read_b128 v[216:219], v198 offset:6144
	ds_read_b128 v[220:223], v198 offset:7168
	global_load_lds_dwordx4 v170, s[50:51]
	s_add_i32 m0, s39, 0xe000
	s_nop 0
	global_load_lds_dwordx4 v172, s[50:51]
	s_waitcnt vmcnt(8)
	s_waitcnt lgkmcnt(0)
	s_barrier
	s_setprio 1
	s_waitcnt lgkmcnt(0)
	v_mfma_i32_16x16x64_i8 v[126:129], v[158:161], v[186:189], v[126:129]
	v_mfma_i32_16x16x64_i8 v[122:125], v[154:157], v[186:189], v[122:125]
	v_mfma_i32_16x16x64_i8 v[110:113], v[158:161], v[200:203], v[110:113]
	v_mfma_i32_16x16x64_i8 v[106:109], v[154:157], v[200:203], v[106:109]
	v_mfma_i32_16x16x64_i8 v[94:97], v[158:161], v[208:211], v[94:97]
	v_mfma_i32_16x16x64_i8 v[90:93], v[154:157], v[208:211], v[90:93]
	v_mfma_i32_16x16x64_i8 v[78:81], v[158:161], v[216:219], v[78:81]
	v_mfma_i32_16x16x64_i8 v[74:77], v[154:157], v[216:219], v[74:77]
	s_nop 0
	v_mfma_i32_16x16x64_i8 v[126:129], v[150:153], v[190:193], v[126:129]
	v_mfma_i32_16x16x64_i8 v[122:125], v[146:149], v[190:193], v[122:125]
	v_mfma_i32_16x16x64_i8 v[110:113], v[150:153], v[204:207], v[110:113]
	v_mfma_i32_16x16x64_i8 v[106:109], v[146:149], v[204:207], v[106:109]
	v_mfma_i32_16x16x64_i8 v[94:97], v[150:153], v[212:215], v[94:97]
	v_mfma_i32_16x16x64_i8 v[90:93], v[146:149], v[212:215], v[90:93]
	v_mfma_i32_16x16x64_i8 v[78:81], v[150:153], v[220:223], v[78:81]
	v_mfma_i32_16x16x64_i8 v[74:77], v[146:149], v[220:223], v[74:77]
	s_setprio 0
	s_setprio 1
	v_mfma_i32_16x16x64_i8 v[118:121], v[142:145], v[186:189], v[118:121]
	v_mfma_i32_16x16x64_i8 v[114:117], v[138:141], v[186:189], v[114:117]
	v_mfma_i32_16x16x64_i8 v[102:105], v[142:145], v[200:203], v[102:105]
	v_mfma_i32_16x16x64_i8 v[98:101], v[138:141], v[200:203], v[98:101]
	v_mfma_i32_16x16x64_i8 v[86:89], v[142:145], v[208:211], v[86:89]
	v_mfma_i32_16x16x64_i8 v[82:85], v[138:141], v[208:211], v[82:85]
	v_mfma_i32_16x16x64_i8 v[70:73], v[142:145], v[216:219], v[70:73]
	v_mfma_i32_16x16x64_i8 v[66:69], v[138:141], v[216:219], v[66:69]
	s_nop 0
	v_mfma_i32_16x16x64_i8 v[118:121], v[130:133], v[190:193], v[118:121]
	v_mfma_i32_16x16x64_i8 v[114:117], v[134:137], v[190:193], v[114:117]
	v_mfma_i32_16x16x64_i8 v[102:105], v[130:133], v[204:207], v[102:105]
	v_mfma_i32_16x16x64_i8 v[98:101], v[134:137], v[204:207], v[98:101]
	v_mfma_i32_16x16x64_i8 v[86:89], v[130:133], v[212:215], v[86:89]
	v_mfma_i32_16x16x64_i8 v[82:85], v[134:137], v[212:215], v[82:85]
	v_mfma_i32_16x16x64_i8 v[70:73], v[130:133], v[220:223], v[70:73]
	v_mfma_i32_16x16x64_i8 v[66:69], v[134:137], v[220:223], v[66:69]
	s_setprio 0
	s_barrier
	s_add_i32 s18, s88, s7
	s_mov_b32 m0, s18
	ds_read_b128 v[200:203], v198 offset:16384
	ds_read_b128 v[204:207], v198 offset:17408
	ds_read_b128 v[208:211], v198 offset:18432
	ds_read_b128 v[212:215], v198 offset:19456
	ds_read_b128 v[216:219], v198 offset:20480
	ds_read_b128 v[220:223], v198 offset:21504
	ds_read_b128 v[224:227], v198 offset:22528
	ds_read_b128 v[228:231], v198 offset:23552
	global_load_lds_dwordx4 v164, s[56:57]
	s_add_i32 m0, s18, 0x2000
	s_add_u32 s18, s56, 0x80000
	s_addc_u32 s19, s57, 0
	s_add_i32 s25, s89, s7
	global_load_lds_dwordx4 v168, s[56:57]
	s_mov_b32 m0, s25
	s_nop 0
	global_load_lds_dwordx4 v164, s[18:19]
	s_add_i32 m0, s25, 0x2000
	s_nop 0
	global_load_lds_dwordx4 v168, s[18:19]
	s_mov_b32 m0, s39
	s_nop 0
	global_load_lds_dwordx4 v162, s[58:59]
	s_mov_b32 m0, s43
	s_nop 0
	global_load_lds_dwordx4 v166, s[58:59]
	s_waitcnt vmcnt(8)
	s_waitcnt lgkmcnt(0)
	s_barrier
	s_setprio 1
	s_waitcnt lgkmcnt(0)
	v_mfma_i32_16x16x64_i8 v[62:65], v[158:161], v[200:203], v[62:65]
	v_mfma_i32_16x16x64_i8 v[58:61], v[154:157], v[200:203], v[58:61]
	v_mfma_i32_16x16x64_i8 v[46:49], v[158:161], v[208:211], v[46:49]
	v_mfma_i32_16x16x64_i8 v[42:45], v[154:157], v[208:211], v[42:45]
	v_mfma_i32_16x16x64_i8 v[30:33], v[158:161], v[216:219], v[30:33]
	v_mfma_i32_16x16x64_i8 v[26:29], v[154:157], v[216:219], v[26:29]
	v_mfma_i32_16x16x64_i8 v[14:17], v[158:161], v[224:227], v[14:17]
	v_mfma_i32_16x16x64_i8 v[10:13], v[154:157], v[224:227], v[10:13]
	s_nop 0
	v_mfma_i32_16x16x64_i8 v[62:65], v[150:153], v[204:207], v[62:65]
	v_mfma_i32_16x16x64_i8 v[58:61], v[146:149], v[204:207], v[58:61]
	v_mfma_i32_16x16x64_i8 v[46:49], v[150:153], v[212:215], v[46:49]
	v_mfma_i32_16x16x64_i8 v[42:45], v[146:149], v[212:215], v[42:45]
	v_mfma_i32_16x16x64_i8 v[30:33], v[150:153], v[220:223], v[30:33]
	v_mfma_i32_16x16x64_i8 v[26:29], v[146:149], v[220:223], v[26:29]
	v_mfma_i32_16x16x64_i8 v[14:17], v[150:153], v[228:231], v[14:17]
	v_mfma_i32_16x16x64_i8 v[10:13], v[146:149], v[228:231], v[10:13]
	s_setprio 0
	s_setprio 1
	v_mfma_i32_16x16x64_i8 v[54:57], v[142:145], v[200:203], v[54:57]
	v_mfma_i32_16x16x64_i8 v[50:53], v[138:141], v[200:203], v[50:53]
	v_mfma_i32_16x16x64_i8 v[38:41], v[142:145], v[208:211], v[38:41]
	v_mfma_i32_16x16x64_i8 v[34:37], v[138:141], v[208:211], v[34:37]
	v_mfma_i32_16x16x64_i8 v[22:25], v[142:145], v[216:219], v[22:25]
	v_mfma_i32_16x16x64_i8 v[18:21], v[138:141], v[216:219], v[18:21]
	v_mfma_i32_16x16x64_i8 v[6:9], v[142:145], v[224:227], v[6:9]
	v_mfma_i32_16x16x64_i8 v[2:5], v[138:141], v[224:227], v[2:5]
	s_nop 0
	v_mfma_i32_16x16x64_i8 v[54:57], v[130:133], v[204:207], v[54:57]
	v_mfma_i32_16x16x64_i8 v[50:53], v[134:137], v[204:207], v[50:53]
	v_mfma_i32_16x16x64_i8 v[38:41], v[130:133], v[212:215], v[38:41]
	v_mfma_i32_16x16x64_i8 v[34:37], v[134:137], v[212:215], v[34:37]
	v_mfma_i32_16x16x64_i8 v[22:25], v[130:133], v[220:223], v[22:25]
	v_mfma_i32_16x16x64_i8 v[18:21], v[134:137], v[220:223], v[18:21]
	v_mfma_i32_16x16x64_i8 v[6:9], v[130:133], v[228:231], v[6:9]
	v_mfma_i32_16x16x64_i8 v[2:5], v[134:137], v[228:231], v[2:5]
	s_setprio 0
	s_barrier
	s_add_i32 s25, 0, 0x18000
	s_add_i32 vcc_lo, 0, 0x1c000
	v_add_u32_e32 v142, s25, v196
	v_add_u32_e32 v158, vcc_lo, v196
	ds_read_b128 v[130:133], v142
	ds_read_b128 v[134:137], v142 offset:1024
	ds_read_b128 v[138:141], v142 offset:2048
	ds_read_b128 v[142:145], v142 offset:3072
	ds_read_b128 v[146:149], v158
	ds_read_b128 v[150:153], v158 offset:1024
	ds_read_b128 v[154:157], v158 offset:2048
	ds_read_b128 v[158:161], v158 offset:3072
	s_add_u32 s18, s58, 0x80000
	s_addc_u32 s19, s59, 0
	s_mov_b32 m0, s61
	ds_read_b128 v[200:203], v198 offset:32768
	ds_read_b128 v[204:207], v198 offset:33792
	ds_read_b128 v[208:211], v198 offset:34816
	ds_read_b128 v[212:215], v198 offset:35840
	ds_read_b128 v[216:219], v198 offset:36864
	ds_read_b128 v[220:223], v198 offset:37888
	ds_read_b128 v[224:227], v198 offset:38912
	ds_read_b128 v[228:231], v198 offset:39936
	global_load_lds_dwordx4 v162, s[18:19]
	s_mov_b32 m0, s62
	s_nop 0
	global_load_lds_dwordx4 v166, s[18:19]
	s_waitcnt vmcnt(8)
	s_waitcnt lgkmcnt(0)
	s_barrier
	s_setprio 1
	s_waitcnt lgkmcnt(0)
	v_mfma_i32_16x16x64_i8 v[126:129], v[130:133], v[200:203], v[126:129]
	v_mfma_i32_16x16x64_i8 v[122:125], v[138:141], v[200:203], v[122:125]
	v_mfma_i32_16x16x64_i8 v[110:113], v[130:133], v[208:211], v[110:113]
	v_mfma_i32_16x16x64_i8 v[106:109], v[138:141], v[208:211], v[106:109]
	v_mfma_i32_16x16x64_i8 v[94:97], v[130:133], v[216:219], v[94:97]
	v_mfma_i32_16x16x64_i8 v[90:93], v[138:141], v[216:219], v[90:93]
	v_mfma_i32_16x16x64_i8 v[78:81], v[130:133], v[224:227], v[78:81]
	v_mfma_i32_16x16x64_i8 v[74:77], v[138:141], v[224:227], v[74:77]
	s_nop 0
	v_mfma_i32_16x16x64_i8 v[126:129], v[134:137], v[204:207], v[126:129]
	v_mfma_i32_16x16x64_i8 v[122:125], v[142:145], v[204:207], v[122:125]
	v_mfma_i32_16x16x64_i8 v[110:113], v[134:137], v[212:215], v[110:113]
	v_mfma_i32_16x16x64_i8 v[106:109], v[142:145], v[212:215], v[106:109]
	v_mfma_i32_16x16x64_i8 v[94:97], v[134:137], v[220:223], v[94:97]
	v_mfma_i32_16x16x64_i8 v[90:93], v[142:145], v[220:223], v[90:93]
	v_mfma_i32_16x16x64_i8 v[78:81], v[134:137], v[228:231], v[78:81]
	v_mfma_i32_16x16x64_i8 v[74:77], v[142:145], v[228:231], v[74:77]
	s_setprio 0
	s_setprio 1
	v_mfma_i32_16x16x64_i8 v[118:121], v[146:149], v[200:203], v[118:121]
	v_mfma_i32_16x16x64_i8 v[114:117], v[154:157], v[200:203], v[114:117]
	v_mfma_i32_16x16x64_i8 v[102:105], v[146:149], v[208:211], v[102:105]
	v_mfma_i32_16x16x64_i8 v[98:101], v[154:157], v[208:211], v[98:101]
	v_mfma_i32_16x16x64_i8 v[86:89], v[146:149], v[216:219], v[86:89]
	v_mfma_i32_16x16x64_i8 v[82:85], v[154:157], v[216:219], v[82:85]
	v_mfma_i32_16x16x64_i8 v[70:73], v[146:149], v[224:227], v[70:73]
	v_mfma_i32_16x16x64_i8 v[66:69], v[154:157], v[224:227], v[66:69]
	s_nop 0
	v_mfma_i32_16x16x64_i8 v[118:121], v[150:153], v[204:207], v[118:121]
	v_mfma_i32_16x16x64_i8 v[114:117], v[158:161], v[204:207], v[114:117]
	v_mfma_i32_16x16x64_i8 v[102:105], v[150:153], v[212:215], v[102:105]
	v_mfma_i32_16x16x64_i8 v[98:101], v[158:161], v[212:215], v[98:101]
	v_mfma_i32_16x16x64_i8 v[86:89], v[150:153], v[220:223], v[86:89]
	v_mfma_i32_16x16x64_i8 v[82:85], v[158:161], v[220:223], v[82:85]
	v_mfma_i32_16x16x64_i8 v[70:73], v[150:153], v[228:231], v[70:73]
	v_mfma_i32_16x16x64_i8 v[66:69], v[158:161], v[228:231], v[66:69]
	s_setprio 0
	s_barrier
	s_add_i32 s18, s25, s7
	s_mov_b32 m0, s18
	s_add_u32 s98, s56, 0x80
	s_addc_u32 s99, s57, 0
	s_add_u32 s100, s58, 0x80
	s_addc_u32 s101, s59, 0
	ds_read_b128 v[200:203], v198 offset:49152
	ds_read_b128 v[204:207], v198 offset:50176
	ds_read_b128 v[208:211], v198 offset:51200
	ds_read_b128 v[212:215], v198 offset:52224
	ds_read_b128 v[216:219], v198 offset:53248
	ds_read_b128 v[220:223], v198 offset:54272
	ds_read_b128 v[224:227], v198 offset:55296
	ds_read_b128 v[228:231], v198 offset:56320
	global_load_lds_dwordx4 v164, s[98:99]
	s_add_i32 m0, s18, 0x2000
	s_add_u32 s18, s56, 0x80080
	s_addc_u32 s19, s57, 0
	s_add_i32 s25, vcc_lo, s7
	global_load_lds_dwordx4 v168, s[98:99]
	s_mov_b32 m0, s25
	s_nop 0
	global_load_lds_dwordx4 v164, s[18:19]
	s_add_i32 m0, s25, 0x2000
	s_nop 0
	global_load_lds_dwordx4 v168, s[18:19]
	s_mov_b32 m0, s67
	s_nop 0
	global_load_lds_dwordx4 v162, s[100:101]
	s_mov_b32 m0, s68
	s_nop 0
	global_load_lds_dwordx4 v166, s[100:101]
	s_waitcnt vmcnt(8)
	s_waitcnt lgkmcnt(0)
	s_barrier
	s_setprio 1
	s_waitcnt lgkmcnt(0)
	v_mfma_i32_16x16x64_i8 v[62:65], v[130:133], v[200:203], v[62:65]
	v_mfma_i32_16x16x64_i8 v[58:61], v[138:141], v[200:203], v[58:61]
	v_mfma_i32_16x16x64_i8 v[46:49], v[130:133], v[208:211], v[46:49]
	v_mfma_i32_16x16x64_i8 v[42:45], v[138:141], v[208:211], v[42:45]
	v_mfma_i32_16x16x64_i8 v[30:33], v[130:133], v[216:219], v[30:33]
	v_mfma_i32_16x16x64_i8 v[26:29], v[138:141], v[216:219], v[26:29]
	v_mfma_i32_16x16x64_i8 v[14:17], v[130:133], v[224:227], v[14:17]
	v_mfma_i32_16x16x64_i8 v[10:13], v[138:141], v[224:227], v[10:13]
	s_nop 0
	v_mfma_i32_16x16x64_i8 v[62:65], v[134:137], v[204:207], v[62:65]
	v_mfma_i32_16x16x64_i8 v[58:61], v[142:145], v[204:207], v[58:61]
	v_mfma_i32_16x16x64_i8 v[46:49], v[134:137], v[212:215], v[46:49]
	v_mfma_i32_16x16x64_i8 v[42:45], v[142:145], v[212:215], v[42:45]
	v_mfma_i32_16x16x64_i8 v[30:33], v[134:137], v[220:223], v[30:33]
	v_mfma_i32_16x16x64_i8 v[26:29], v[142:145], v[220:223], v[26:29]
	v_mfma_i32_16x16x64_i8 v[14:17], v[134:137], v[228:231], v[14:17]
	v_mfma_i32_16x16x64_i8 v[10:13], v[142:145], v[228:231], v[10:13]
	s_setprio 0
	s_setprio 1
	v_mfma_i32_16x16x64_i8 v[54:57], v[146:149], v[200:203], v[54:57]
	v_mfma_i32_16x16x64_i8 v[50:53], v[154:157], v[200:203], v[50:53]
	v_mfma_i32_16x16x64_i8 v[38:41], v[146:149], v[208:211], v[38:41]
	v_mfma_i32_16x16x64_i8 v[34:37], v[154:157], v[208:211], v[34:37]
	v_mfma_i32_16x16x64_i8 v[22:25], v[146:149], v[216:219], v[22:25]
	v_mfma_i32_16x16x64_i8 v[18:21], v[154:157], v[216:219], v[18:21]
	v_mfma_i32_16x16x64_i8 v[6:9], v[146:149], v[224:227], v[6:9]
	v_mfma_i32_16x16x64_i8 v[2:5], v[154:157], v[224:227], v[2:5]
	s_nop 0
	v_mfma_i32_16x16x64_i8 v[54:57], v[150:153], v[204:207], v[54:57]
	v_mfma_i32_16x16x64_i8 v[50:53], v[158:161], v[204:207], v[50:53]
	v_mfma_i32_16x16x64_i8 v[38:41], v[150:153], v[212:215], v[38:41]
	v_mfma_i32_16x16x64_i8 v[34:37], v[158:161], v[212:215], v[34:37]
	v_mfma_i32_16x16x64_i8 v[22:25], v[150:153], v[220:223], v[22:25]
	v_mfma_i32_16x16x64_i8 v[18:21], v[158:161], v[220:223], v[18:21]
	v_mfma_i32_16x16x64_i8 v[6:9], v[150:153], v[228:231], v[6:9]
	v_mfma_i32_16x16x64_i8 v[2:5], v[158:161], v[228:231], v[2:5]
	s_setprio 0
	s_barrier
	s_add_i32 s65, s65, 2
	s_add_u32 s50, s50, 0x100
	s_addc_u32 s51, s51, 0
	s_add_u32 s92, s92, 0x100
	s_addc_u32 s64, s64, 0
	s_cmp_gt_u32 s65, 29
	s_cbranch_scc1 .LBB0_219
